# speedup vs baseline: 1.0416x; 1.0416x over previous
_Z13reduce_kernelPKDF16_Pf:
	v_cmp_gt_u32_e32 vcc, 0x80, v0
	s_load_dwordx4 s[4:7], s[0:1], 0x0
	s_and_b64 s[8:9], vcc, exec
	s_cbranch_scc0 .Lk3_exit
	v_lshl_or_b32 v2, s2, 7, v0
	v_lshlrev_b32_e32 v1, 4, v2
	s_waitcnt lgkmcnt(0)
	global_load_dwordx4 v[16:19], v1, s[4:5] nt
	s_add_u32 s4, s4, 0x40000
	s_addc_u32 s5, s5, 0
	global_load_dwordx4 v[20:23], v1, s[4:5] nt
	s_add_u32 s4, s4, 0x40000
	s_addc_u32 s5, s5, 0
	global_load_dwordx4 v[24:27], v1, s[4:5] nt
	s_add_u32 s4, s4, 0x40000
	s_addc_u32 s5, s5, 0
	global_load_dwordx4 v[28:31], v1, s[4:5] nt
	s_add_u32 s4, s4, 0x40000
	s_addc_u32 s5, s5, 0
	global_load_dwordx4 v[32:35], v1, s[4:5] nt
	s_add_u32 s4, s4, 0x40000
	s_addc_u32 s5, s5, 0
	global_load_dwordx4 v[36:39], v1, s[4:5] nt
	s_add_u32 s4, s4, 0x40000
	s_addc_u32 s5, s5, 0
	global_load_dwordx4 v[40:43], v1, s[4:5] nt
	s_add_u32 s4, s4, 0x40000
	s_addc_u32 s5, s5, 0
	global_load_dwordx4 v[44:47], v1, s[4:5] nt
	s_add_u32 s4, s4, 0x40000
	s_addc_u32 s5, s5, 0
	global_load_dwordx4 v[48:51], v1, s[4:5] nt
	s_add_u32 s4, s4, 0x40000
	s_addc_u32 s5, s5, 0
	global_load_dwordx4 v[52:55], v1, s[4:5] nt
	s_add_u32 s4, s4, 0x40000
	s_addc_u32 s5, s5, 0
	global_load_dwordx4 v[56:59], v1, s[4:5] nt
	s_add_u32 s4, s4, 0x40000
	s_addc_u32 s5, s5, 0
	global_load_dwordx4 v[60:63], v1, s[4:5] nt
	s_add_u32 s4, s4, 0x40000
	s_addc_u32 s5, s5, 0
	global_load_dwordx4 v[64:67], v1, s[4:5] nt
	s_add_u32 s4, s4, 0x40000
	s_addc_u32 s5, s5, 0
	global_load_dwordx4 v[68:71], v1, s[4:5] nt
	s_add_u32 s4, s4, 0x40000
	s_addc_u32 s5, s5, 0
	global_load_dwordx4 v[72:75], v1, s[4:5] nt
	s_add_u32 s4, s4, 0x40000
	s_addc_u32 s5, s5, 0
	global_load_dwordx4 v[76:79], v1, s[4:5] nt
	s_add_u32 s4, s4, 0x40000
	s_addc_u32 s5, s5, 0
	global_load_dwordx4 v[80:83], v1, s[4:5] nt
	s_add_u32 s4, s4, 0x40000
	s_addc_u32 s5, s5, 0
	global_load_dwordx4 v[84:87], v1, s[4:5] nt
	s_add_u32 s4, s4, 0x40000
	s_addc_u32 s5, s5, 0
	global_load_dwordx4 v[88:91], v1, s[4:5] nt
	s_add_u32 s4, s4, 0x40000
	s_addc_u32 s5, s5, 0
	global_load_dwordx4 v[92:95], v1, s[4:5] nt
	s_add_u32 s4, s4, 0x40000
	s_addc_u32 s5, s5, 0
	global_load_dwordx4 v[96:99], v1, s[4:5] nt
	s_add_u32 s4, s4, 0x40000
	s_addc_u32 s5, s5, 0
	global_load_dwordx4 v[100:103], v1, s[4:5] nt
	s_add_u32 s4, s4, 0x40000
	s_addc_u32 s5, s5, 0
	global_load_dwordx4 v[104:107], v1, s[4:5] nt
	s_add_u32 s4, s4, 0x40000
	s_addc_u32 s5, s5, 0
	global_load_dwordx4 v[108:111], v1, s[4:5] nt
	s_add_u32 s4, s4, 0x40000
	s_addc_u32 s5, s5, 0
	global_load_dwordx4 v[112:115], v1, s[4:5] nt
	s_add_u32 s4, s4, 0x40000
	s_addc_u32 s5, s5, 0
	global_load_dwordx4 v[116:119], v1, s[4:5] nt
	s_add_u32 s4, s4, 0x40000
	s_addc_u32 s5, s5, 0
	global_load_dwordx4 v[120:123], v1, s[4:5] nt
	s_add_u32 s4, s4, 0x40000
	s_addc_u32 s5, s5, 0
	global_load_dwordx4 v[124:127], v1, s[4:5] nt
	s_add_u32 s4, s4, 0x40000
	s_addc_u32 s5, s5, 0
	global_load_dwordx4 v[128:131], v1, s[4:5] nt
	s_add_u32 s4, s4, 0x40000
	s_addc_u32 s5, s5, 0
	global_load_dwordx4 v[132:135], v1, s[4:5] nt
	s_add_u32 s4, s4, 0x40000
	s_addc_u32 s5, s5, 0
	global_load_dwordx4 v[136:139], v1, s[4:5] nt
	s_add_u32 s4, s4, 0x40000
	s_addc_u32 s5, s5, 0
	global_load_dwordx4 v[140:143], v1, s[4:5] nt
	v_mov_b64_e32 v[4:5], 0
	v_mov_b64_e32 v[6:7], 0
	v_mov_b64_e32 v[8:9], 0
	v_mov_b64_e32 v[10:11], 0
	s_waitcnt vmcnt(31)
	v_cvt_f32_f16_e32 v144, v16
	v_cvt_f32_f16_sdwa v145, v16 dst_sel:DWORD dst_unused:UNUSED_PAD src0_sel:WORD_1
	v_cvt_f32_f16_e32 v146, v17
	v_cvt_f32_f16_sdwa v147, v17 dst_sel:DWORD dst_unused:UNUSED_PAD src0_sel:WORD_1
	v_cvt_f32_f16_e32 v148, v18
	v_cvt_f32_f16_sdwa v149, v18 dst_sel:DWORD dst_unused:UNUSED_PAD src0_sel:WORD_1
	v_cvt_f32_f16_e32 v150, v19
	v_cvt_f32_f16_sdwa v151, v19 dst_sel:DWORD dst_unused:UNUSED_PAD src0_sel:WORD_1
	v_pk_add_f32 v[4:5], v[4:5], v[144:145]
	v_pk_add_f32 v[6:7], v[6:7], v[146:147]
	v_pk_add_f32 v[8:9], v[8:9], v[148:149]
	v_pk_add_f32 v[10:11], v[10:11], v[150:151]
	s_waitcnt vmcnt(30)
	v_cvt_f32_f16_e32 v144, v20
	v_cvt_f32_f16_sdwa v145, v20 dst_sel:DWORD dst_unused:UNUSED_PAD src0_sel:WORD_1
	v_cvt_f32_f16_e32 v146, v21
	v_cvt_f32_f16_sdwa v147, v21 dst_sel:DWORD dst_unused:UNUSED_PAD src0_sel:WORD_1
	v_cvt_f32_f16_e32 v148, v22
	v_cvt_f32_f16_sdwa v149, v22 dst_sel:DWORD dst_unused:UNUSED_PAD src0_sel:WORD_1
	v_cvt_f32_f16_e32 v150, v23
	v_cvt_f32_f16_sdwa v151, v23 dst_sel:DWORD dst_unused:UNUSED_PAD src0_sel:WORD_1
	v_pk_add_f32 v[4:5], v[4:5], v[144:145]
	v_pk_add_f32 v[6:7], v[6:7], v[146:147]
	v_pk_add_f32 v[8:9], v[8:9], v[148:149]
	v_pk_add_f32 v[10:11], v[10:11], v[150:151]
	s_waitcnt vmcnt(29)
	v_cvt_f32_f16_e32 v144, v24
	v_cvt_f32_f16_sdwa v145, v24 dst_sel:DWORD dst_unused:UNUSED_PAD src0_sel:WORD_1
	v_cvt_f32_f16_e32 v146, v25
	v_cvt_f32_f16_sdwa v147, v25 dst_sel:DWORD dst_unused:UNUSED_PAD src0_sel:WORD_1
	v_cvt_f32_f16_e32 v148, v26
	v_cvt_f32_f16_sdwa v149, v26 dst_sel:DWORD dst_unused:UNUSED_PAD src0_sel:WORD_1
	v_cvt_f32_f16_e32 v150, v27
	v_cvt_f32_f16_sdwa v151, v27 dst_sel:DWORD dst_unused:UNUSED_PAD src0_sel:WORD_1
	v_pk_add_f32 v[4:5], v[4:5], v[144:145]
	v_pk_add_f32 v[6:7], v[6:7], v[146:147]
	v_pk_add_f32 v[8:9], v[8:9], v[148:149]
	v_pk_add_f32 v[10:11], v[10:11], v[150:151]
	s_waitcnt vmcnt(28)
	v_cvt_f32_f16_e32 v144, v28
	v_cvt_f32_f16_sdwa v145, v28 dst_sel:DWORD dst_unused:UNUSED_PAD src0_sel:WORD_1
	v_cvt_f32_f16_e32 v146, v29
	v_cvt_f32_f16_sdwa v147, v29 dst_sel:DWORD dst_unused:UNUSED_PAD src0_sel:WORD_1
	v_cvt_f32_f16_e32 v148, v30
	v_cvt_f32_f16_sdwa v149, v30 dst_sel:DWORD dst_unused:UNUSED_PAD src0_sel:WORD_1
	v_cvt_f32_f16_e32 v150, v31
	v_cvt_f32_f16_sdwa v151, v31 dst_sel:DWORD dst_unused:UNUSED_PAD src0_sel:WORD_1
	v_pk_add_f32 v[4:5], v[4:5], v[144:145]
	v_pk_add_f32 v[6:7], v[6:7], v[146:147]
	v_pk_add_f32 v[8:9], v[8:9], v[148:149]
	v_pk_add_f32 v[10:11], v[10:11], v[150:151]
	s_waitcnt vmcnt(27)
	v_cvt_f32_f16_e32 v144, v32
	v_cvt_f32_f16_sdwa v145, v32 dst_sel:DWORD dst_unused:UNUSED_PAD src0_sel:WORD_1
	v_cvt_f32_f16_e32 v146, v33
	v_cvt_f32_f16_sdwa v147, v33 dst_sel:DWORD dst_unused:UNUSED_PAD src0_sel:WORD_1
	v_cvt_f32_f16_e32 v148, v34
	v_cvt_f32_f16_sdwa v149, v34 dst_sel:DWORD dst_unused:UNUSED_PAD src0_sel:WORD_1
	v_cvt_f32_f16_e32 v150, v35
	v_cvt_f32_f16_sdwa v151, v35 dst_sel:DWORD dst_unused:UNUSED_PAD src0_sel:WORD_1
	v_pk_add_f32 v[4:5], v[4:5], v[144:145]
	v_pk_add_f32 v[6:7], v[6:7], v[146:147]
	v_pk_add_f32 v[8:9], v[8:9], v[148:149]
	v_pk_add_f32 v[10:11], v[10:11], v[150:151]
	s_waitcnt vmcnt(26)
	v_cvt_f32_f16_e32 v144, v36
	v_cvt_f32_f16_sdwa v145, v36 dst_sel:DWORD dst_unused:UNUSED_PAD src0_sel:WORD_1
	v_cvt_f32_f16_e32 v146, v37
	v_cvt_f32_f16_sdwa v147, v37 dst_sel:DWORD dst_unused:UNUSED_PAD src0_sel:WORD_1
	v_cvt_f32_f16_e32 v148, v38
	v_cvt_f32_f16_sdwa v149, v38 dst_sel:DWORD dst_unused:UNUSED_PAD src0_sel:WORD_1
	v_cvt_f32_f16_e32 v150, v39
	v_cvt_f32_f16_sdwa v151, v39 dst_sel:DWORD dst_unused:UNUSED_PAD src0_sel:WORD_1
	v_pk_add_f32 v[4:5], v[4:5], v[144:145]
	v_pk_add_f32 v[6:7], v[6:7], v[146:147]
	v_pk_add_f32 v[8:9], v[8:9], v[148:149]
	v_pk_add_f32 v[10:11], v[10:11], v[150:151]
	s_waitcnt vmcnt(25)
	v_cvt_f32_f16_e32 v144, v40
	v_cvt_f32_f16_sdwa v145, v40 dst_sel:DWORD dst_unused:UNUSED_PAD src0_sel:WORD_1
	v_cvt_f32_f16_e32 v146, v41
	v_cvt_f32_f16_sdwa v147, v41 dst_sel:DWORD dst_unused:UNUSED_PAD src0_sel:WORD_1
	v_cvt_f32_f16_e32 v148, v42
	v_cvt_f32_f16_sdwa v149, v42 dst_sel:DWORD dst_unused:UNUSED_PAD src0_sel:WORD_1
	v_cvt_f32_f16_e32 v150, v43
	v_cvt_f32_f16_sdwa v151, v43 dst_sel:DWORD dst_unused:UNUSED_PAD src0_sel:WORD_1
	v_pk_add_f32 v[4:5], v[4:5], v[144:145]
	v_pk_add_f32 v[6:7], v[6:7], v[146:147]
	v_pk_add_f32 v[8:9], v[8:9], v[148:149]
	v_pk_add_f32 v[10:11], v[10:11], v[150:151]
	s_waitcnt vmcnt(24)
	v_cvt_f32_f16_e32 v144, v44
	v_cvt_f32_f16_sdwa v145, v44 dst_sel:DWORD dst_unused:UNUSED_PAD src0_sel:WORD_1
	v_cvt_f32_f16_e32 v146, v45
	v_cvt_f32_f16_sdwa v147, v45 dst_sel:DWORD dst_unused:UNUSED_PAD src0_sel:WORD_1
	v_cvt_f32_f16_e32 v148, v46
	v_cvt_f32_f16_sdwa v149, v46 dst_sel:DWORD dst_unused:UNUSED_PAD src0_sel:WORD_1
	v_cvt_f32_f16_e32 v150, v47
	v_cvt_f32_f16_sdwa v151, v47 dst_sel:DWORD dst_unused:UNUSED_PAD src0_sel:WORD_1
	v_pk_add_f32 v[4:5], v[4:5], v[144:145]
	v_pk_add_f32 v[6:7], v[6:7], v[146:147]
	v_pk_add_f32 v[8:9], v[8:9], v[148:149]
	v_pk_add_f32 v[10:11], v[10:11], v[150:151]
	s_waitcnt vmcnt(23)
	v_cvt_f32_f16_e32 v144, v48
	v_cvt_f32_f16_sdwa v145, v48 dst_sel:DWORD dst_unused:UNUSED_PAD src0_sel:WORD_1
	v_cvt_f32_f16_e32 v146, v49
	v_cvt_f32_f16_sdwa v147, v49 dst_sel:DWORD dst_unused:UNUSED_PAD src0_sel:WORD_1
	v_cvt_f32_f16_e32 v148, v50
	v_cvt_f32_f16_sdwa v149, v50 dst_sel:DWORD dst_unused:UNUSED_PAD src0_sel:WORD_1
	v_cvt_f32_f16_e32 v150, v51
	v_cvt_f32_f16_sdwa v151, v51 dst_sel:DWORD dst_unused:UNUSED_PAD src0_sel:WORD_1
	v_pk_add_f32 v[4:5], v[4:5], v[144:145]
	v_pk_add_f32 v[6:7], v[6:7], v[146:147]
	v_pk_add_f32 v[8:9], v[8:9], v[148:149]
	v_pk_add_f32 v[10:11], v[10:11], v[150:151]
	s_waitcnt vmcnt(22)
	v_cvt_f32_f16_e32 v144, v52
	v_cvt_f32_f16_sdwa v145, v52 dst_sel:DWORD dst_unused:UNUSED_PAD src0_sel:WORD_1
	v_cvt_f32_f16_e32 v146, v53
	v_cvt_f32_f16_sdwa v147, v53 dst_sel:DWORD dst_unused:UNUSED_PAD src0_sel:WORD_1
	v_cvt_f32_f16_e32 v148, v54
	v_cvt_f32_f16_sdwa v149, v54 dst_sel:DWORD dst_unused:UNUSED_PAD src0_sel:WORD_1
	v_cvt_f32_f16_e32 v150, v55
	v_cvt_f32_f16_sdwa v151, v55 dst_sel:DWORD dst_unused:UNUSED_PAD src0_sel:WORD_1
	v_pk_add_f32 v[4:5], v[4:5], v[144:145]
	v_pk_add_f32 v[6:7], v[6:7], v[146:147]
	v_pk_add_f32 v[8:9], v[8:9], v[148:149]
	v_pk_add_f32 v[10:11], v[10:11], v[150:151]
	s_waitcnt vmcnt(21)
	v_cvt_f32_f16_e32 v144, v56
	v_cvt_f32_f16_sdwa v145, v56 dst_sel:DWORD dst_unused:UNUSED_PAD src0_sel:WORD_1
	v_cvt_f32_f16_e32 v146, v57
	v_cvt_f32_f16_sdwa v147, v57 dst_sel:DWORD dst_unused:UNUSED_PAD src0_sel:WORD_1
	v_cvt_f32_f16_e32 v148, v58
	v_cvt_f32_f16_sdwa v149, v58 dst_sel:DWORD dst_unused:UNUSED_PAD src0_sel:WORD_1
	v_cvt_f32_f16_e32 v150, v59
	v_cvt_f32_f16_sdwa v151, v59 dst_sel:DWORD dst_unused:UNUSED_PAD src0_sel:WORD_1
	v_pk_add_f32 v[4:5], v[4:5], v[144:145]
	v_pk_add_f32 v[6:7], v[6:7], v[146:147]
	v_pk_add_f32 v[8:9], v[8:9], v[148:149]
	v_pk_add_f32 v[10:11], v[10:11], v[150:151]
	s_waitcnt vmcnt(20)
	v_cvt_f32_f16_e32 v144, v60
	v_cvt_f32_f16_sdwa v145, v60 dst_sel:DWORD dst_unused:UNUSED_PAD src0_sel:WORD_1
	v_cvt_f32_f16_e32 v146, v61
	v_cvt_f32_f16_sdwa v147, v61 dst_sel:DWORD dst_unused:UNUSED_PAD src0_sel:WORD_1
	v_cvt_f32_f16_e32 v148, v62
	v_cvt_f32_f16_sdwa v149, v62 dst_sel:DWORD dst_unused:UNUSED_PAD src0_sel:WORD_1
	v_cvt_f32_f16_e32 v150, v63
	v_cvt_f32_f16_sdwa v151, v63 dst_sel:DWORD dst_unused:UNUSED_PAD src0_sel:WORD_1
	v_pk_add_f32 v[4:5], v[4:5], v[144:145]
	v_pk_add_f32 v[6:7], v[6:7], v[146:147]
	v_pk_add_f32 v[8:9], v[8:9], v[148:149]
	v_pk_add_f32 v[10:11], v[10:11], v[150:151]
	s_waitcnt vmcnt(19)
	v_cvt_f32_f16_e32 v144, v64
	v_cvt_f32_f16_sdwa v145, v64 dst_sel:DWORD dst_unused:UNUSED_PAD src0_sel:WORD_1
	v_cvt_f32_f16_e32 v146, v65
	v_cvt_f32_f16_sdwa v147, v65 dst_sel:DWORD dst_unused:UNUSED_PAD src0_sel:WORD_1
	v_cvt_f32_f16_e32 v148, v66
	v_cvt_f32_f16_sdwa v149, v66 dst_sel:DWORD dst_unused:UNUSED_PAD src0_sel:WORD_1
	v_cvt_f32_f16_e32 v150, v67
	v_cvt_f32_f16_sdwa v151, v67 dst_sel:DWORD dst_unused:UNUSED_PAD src0_sel:WORD_1
	v_pk_add_f32 v[4:5], v[4:5], v[144:145]
	v_pk_add_f32 v[6:7], v[6:7], v[146:147]
	v_pk_add_f32 v[8:9], v[8:9], v[148:149]
	v_pk_add_f32 v[10:11], v[10:11], v[150:151]
	s_waitcnt vmcnt(18)
	v_cvt_f32_f16_e32 v144, v68
	v_cvt_f32_f16_sdwa v145, v68 dst_sel:DWORD dst_unused:UNUSED_PAD src0_sel:WORD_1
	v_cvt_f32_f16_e32 v146, v69
	v_cvt_f32_f16_sdwa v147, v69 dst_sel:DWORD dst_unused:UNUSED_PAD src0_sel:WORD_1
	v_cvt_f32_f16_e32 v148, v70
	v_cvt_f32_f16_sdwa v149, v70 dst_sel:DWORD dst_unused:UNUSED_PAD src0_sel:WORD_1
	v_cvt_f32_f16_e32 v150, v71
	v_cvt_f32_f16_sdwa v151, v71 dst_sel:DWORD dst_unused:UNUSED_PAD src0_sel:WORD_1
	v_pk_add_f32 v[4:5], v[4:5], v[144:145]
	v_pk_add_f32 v[6:7], v[6:7], v[146:147]
	v_pk_add_f32 v[8:9], v[8:9], v[148:149]
	v_pk_add_f32 v[10:11], v[10:11], v[150:151]
	s_waitcnt vmcnt(17)
	v_cvt_f32_f16_e32 v144, v72
	v_cvt_f32_f16_sdwa v145, v72 dst_sel:DWORD dst_unused:UNUSED_PAD src0_sel:WORD_1
	v_cvt_f32_f16_e32 v146, v73
	v_cvt_f32_f16_sdwa v147, v73 dst_sel:DWORD dst_unused:UNUSED_PAD src0_sel:WORD_1
	v_cvt_f32_f16_e32 v148, v74
	v_cvt_f32_f16_sdwa v149, v74 dst_sel:DWORD dst_unused:UNUSED_PAD src0_sel:WORD_1
	v_cvt_f32_f16_e32 v150, v75
	v_cvt_f32_f16_sdwa v151, v75 dst_sel:DWORD dst_unused:UNUSED_PAD src0_sel:WORD_1
	v_pk_add_f32 v[4:5], v[4:5], v[144:145]
	v_pk_add_f32 v[6:7], v[6:7], v[146:147]
	v_pk_add_f32 v[8:9], v[8:9], v[148:149]
	v_pk_add_f32 v[10:11], v[10:11], v[150:151]
	s_waitcnt vmcnt(16)
	v_cvt_f32_f16_e32 v144, v76
	v_cvt_f32_f16_sdwa v145, v76 dst_sel:DWORD dst_unused:UNUSED_PAD src0_sel:WORD_1
	v_cvt_f32_f16_e32 v146, v77
	v_cvt_f32_f16_sdwa v147, v77 dst_sel:DWORD dst_unused:UNUSED_PAD src0_sel:WORD_1
	v_cvt_f32_f16_e32 v148, v78
	v_cvt_f32_f16_sdwa v149, v78 dst_sel:DWORD dst_unused:UNUSED_PAD src0_sel:WORD_1
	v_cvt_f32_f16_e32 v150, v79
	v_cvt_f32_f16_sdwa v151, v79 dst_sel:DWORD dst_unused:UNUSED_PAD src0_sel:WORD_1
	v_pk_add_f32 v[4:5], v[4:5], v[144:145]
	v_pk_add_f32 v[6:7], v[6:7], v[146:147]
	v_pk_add_f32 v[8:9], v[8:9], v[148:149]
	v_pk_add_f32 v[10:11], v[10:11], v[150:151]
	s_waitcnt vmcnt(15)
	v_cvt_f32_f16_e32 v144, v80
	v_cvt_f32_f16_sdwa v145, v80 dst_sel:DWORD dst_unused:UNUSED_PAD src0_sel:WORD_1
	v_cvt_f32_f16_e32 v146, v81
	v_cvt_f32_f16_sdwa v147, v81 dst_sel:DWORD dst_unused:UNUSED_PAD src0_sel:WORD_1
	v_cvt_f32_f16_e32 v148, v82
	v_cvt_f32_f16_sdwa v149, v82 dst_sel:DWORD dst_unused:UNUSED_PAD src0_sel:WORD_1
	v_cvt_f32_f16_e32 v150, v83
	v_cvt_f32_f16_sdwa v151, v83 dst_sel:DWORD dst_unused:UNUSED_PAD src0_sel:WORD_1
	v_pk_add_f32 v[4:5], v[4:5], v[144:145]
	v_pk_add_f32 v[6:7], v[6:7], v[146:147]
	v_pk_add_f32 v[8:9], v[8:9], v[148:149]
	v_pk_add_f32 v[10:11], v[10:11], v[150:151]
	s_waitcnt vmcnt(14)
	v_cvt_f32_f16_e32 v144, v84
	v_cvt_f32_f16_sdwa v145, v84 dst_sel:DWORD dst_unused:UNUSED_PAD src0_sel:WORD_1
	v_cvt_f32_f16_e32 v146, v85
	v_cvt_f32_f16_sdwa v147, v85 dst_sel:DWORD dst_unused:UNUSED_PAD src0_sel:WORD_1
	v_cvt_f32_f16_e32 v148, v86
	v_cvt_f32_f16_sdwa v149, v86 dst_sel:DWORD dst_unused:UNUSED_PAD src0_sel:WORD_1
	v_cvt_f32_f16_e32 v150, v87
	v_cvt_f32_f16_sdwa v151, v87 dst_sel:DWORD dst_unused:UNUSED_PAD src0_sel:WORD_1
	v_pk_add_f32 v[4:5], v[4:5], v[144:145]
	v_pk_add_f32 v[6:7], v[6:7], v[146:147]
	v_pk_add_f32 v[8:9], v[8:9], v[148:149]
	v_pk_add_f32 v[10:11], v[10:11], v[150:151]
	s_waitcnt vmcnt(13)
	v_cvt_f32_f16_e32 v144, v88
	v_cvt_f32_f16_sdwa v145, v88 dst_sel:DWORD dst_unused:UNUSED_PAD src0_sel:WORD_1
	v_cvt_f32_f16_e32 v146, v89
	v_cvt_f32_f16_sdwa v147, v89 dst_sel:DWORD dst_unused:UNUSED_PAD src0_sel:WORD_1
	v_cvt_f32_f16_e32 v148, v90
	v_cvt_f32_f16_sdwa v149, v90 dst_sel:DWORD dst_unused:UNUSED_PAD src0_sel:WORD_1
	v_cvt_f32_f16_e32 v150, v91
	v_cvt_f32_f16_sdwa v151, v91 dst_sel:DWORD dst_unused:UNUSED_PAD src0_sel:WORD_1
	v_pk_add_f32 v[4:5], v[4:5], v[144:145]
	v_pk_add_f32 v[6:7], v[6:7], v[146:147]
	v_pk_add_f32 v[8:9], v[8:9], v[148:149]
	v_pk_add_f32 v[10:11], v[10:11], v[150:151]
	s_waitcnt vmcnt(12)
	v_cvt_f32_f16_e32 v144, v92
	v_cvt_f32_f16_sdwa v145, v92 dst_sel:DWORD dst_unused:UNUSED_PAD src0_sel:WORD_1
	v_cvt_f32_f16_e32 v146, v93
	v_cvt_f32_f16_sdwa v147, v93 dst_sel:DWORD dst_unused:UNUSED_PAD src0_sel:WORD_1
	v_cvt_f32_f16_e32 v148, v94
	v_cvt_f32_f16_sdwa v149, v94 dst_sel:DWORD dst_unused:UNUSED_PAD src0_sel:WORD_1
	v_cvt_f32_f16_e32 v150, v95
	v_cvt_f32_f16_sdwa v151, v95 dst_sel:DWORD dst_unused:UNUSED_PAD src0_sel:WORD_1
	v_pk_add_f32 v[4:5], v[4:5], v[144:145]
	v_pk_add_f32 v[6:7], v[6:7], v[146:147]
	v_pk_add_f32 v[8:9], v[8:9], v[148:149]
	v_pk_add_f32 v[10:11], v[10:11], v[150:151]
	s_waitcnt vmcnt(11)
	v_cvt_f32_f16_e32 v144, v96
	v_cvt_f32_f16_sdwa v145, v96 dst_sel:DWORD dst_unused:UNUSED_PAD src0_sel:WORD_1
	v_cvt_f32_f16_e32 v146, v97
	v_cvt_f32_f16_sdwa v147, v97 dst_sel:DWORD dst_unused:UNUSED_PAD src0_sel:WORD_1
	v_cvt_f32_f16_e32 v148, v98
	v_cvt_f32_f16_sdwa v149, v98 dst_sel:DWORD dst_unused:UNUSED_PAD src0_sel:WORD_1
	v_cvt_f32_f16_e32 v150, v99
	v_cvt_f32_f16_sdwa v151, v99 dst_sel:DWORD dst_unused:UNUSED_PAD src0_sel:WORD_1
	v_pk_add_f32 v[4:5], v[4:5], v[144:145]
	v_pk_add_f32 v[6:7], v[6:7], v[146:147]
	v_pk_add_f32 v[8:9], v[8:9], v[148:149]
	v_pk_add_f32 v[10:11], v[10:11], v[150:151]
	s_waitcnt vmcnt(10)
	v_cvt_f32_f16_e32 v144, v100
	v_cvt_f32_f16_sdwa v145, v100 dst_sel:DWORD dst_unused:UNUSED_PAD src0_sel:WORD_1
	v_cvt_f32_f16_e32 v146, v101
	v_cvt_f32_f16_sdwa v147, v101 dst_sel:DWORD dst_unused:UNUSED_PAD src0_sel:WORD_1
	v_cvt_f32_f16_e32 v148, v102
	v_cvt_f32_f16_sdwa v149, v102 dst_sel:DWORD dst_unused:UNUSED_PAD src0_sel:WORD_1
	v_cvt_f32_f16_e32 v150, v103
	v_cvt_f32_f16_sdwa v151, v103 dst_sel:DWORD dst_unused:UNUSED_PAD src0_sel:WORD_1
	v_pk_add_f32 v[4:5], v[4:5], v[144:145]
	v_pk_add_f32 v[6:7], v[6:7], v[146:147]
	v_pk_add_f32 v[8:9], v[8:9], v[148:149]
	v_pk_add_f32 v[10:11], v[10:11], v[150:151]
	s_waitcnt vmcnt(9)
	v_cvt_f32_f16_e32 v144, v104
	v_cvt_f32_f16_sdwa v145, v104 dst_sel:DWORD dst_unused:UNUSED_PAD src0_sel:WORD_1
	v_cvt_f32_f16_e32 v146, v105
	v_cvt_f32_f16_sdwa v147, v105 dst_sel:DWORD dst_unused:UNUSED_PAD src0_sel:WORD_1
	v_cvt_f32_f16_e32 v148, v106
	v_cvt_f32_f16_sdwa v149, v106 dst_sel:DWORD dst_unused:UNUSED_PAD src0_sel:WORD_1
	v_cvt_f32_f16_e32 v150, v107
	v_cvt_f32_f16_sdwa v151, v107 dst_sel:DWORD dst_unused:UNUSED_PAD src0_sel:WORD_1
	v_pk_add_f32 v[4:5], v[4:5], v[144:145]
	v_pk_add_f32 v[6:7], v[6:7], v[146:147]
	v_pk_add_f32 v[8:9], v[8:9], v[148:149]
	v_pk_add_f32 v[10:11], v[10:11], v[150:151]
	s_waitcnt vmcnt(8)
	v_cvt_f32_f16_e32 v144, v108
	v_cvt_f32_f16_sdwa v145, v108 dst_sel:DWORD dst_unused:UNUSED_PAD src0_sel:WORD_1
	v_cvt_f32_f16_e32 v146, v109
	v_cvt_f32_f16_sdwa v147, v109 dst_sel:DWORD dst_unused:UNUSED_PAD src0_sel:WORD_1
	v_cvt_f32_f16_e32 v148, v110
	v_cvt_f32_f16_sdwa v149, v110 dst_sel:DWORD dst_unused:UNUSED_PAD src0_sel:WORD_1
	v_cvt_f32_f16_e32 v150, v111
	v_cvt_f32_f16_sdwa v151, v111 dst_sel:DWORD dst_unused:UNUSED_PAD src0_sel:WORD_1
	v_pk_add_f32 v[4:5], v[4:5], v[144:145]
	v_pk_add_f32 v[6:7], v[6:7], v[146:147]
	v_pk_add_f32 v[8:9], v[8:9], v[148:149]
	v_pk_add_f32 v[10:11], v[10:11], v[150:151]
	s_waitcnt vmcnt(7)
	v_cvt_f32_f16_e32 v144, v112
	v_cvt_f32_f16_sdwa v145, v112 dst_sel:DWORD dst_unused:UNUSED_PAD src0_sel:WORD_1
	v_cvt_f32_f16_e32 v146, v113
	v_cvt_f32_f16_sdwa v147, v113 dst_sel:DWORD dst_unused:UNUSED_PAD src0_sel:WORD_1
	v_cvt_f32_f16_e32 v148, v114
	v_cvt_f32_f16_sdwa v149, v114 dst_sel:DWORD dst_unused:UNUSED_PAD src0_sel:WORD_1
	v_cvt_f32_f16_e32 v150, v115
	v_cvt_f32_f16_sdwa v151, v115 dst_sel:DWORD dst_unused:UNUSED_PAD src0_sel:WORD_1
	v_pk_add_f32 v[4:5], v[4:5], v[144:145]
	v_pk_add_f32 v[6:7], v[6:7], v[146:147]
	v_pk_add_f32 v[8:9], v[8:9], v[148:149]
	v_pk_add_f32 v[10:11], v[10:11], v[150:151]
	s_waitcnt vmcnt(6)
	v_cvt_f32_f16_e32 v144, v116
	v_cvt_f32_f16_sdwa v145, v116 dst_sel:DWORD dst_unused:UNUSED_PAD src0_sel:WORD_1
	v_cvt_f32_f16_e32 v146, v117
	v_cvt_f32_f16_sdwa v147, v117 dst_sel:DWORD dst_unused:UNUSED_PAD src0_sel:WORD_1
	v_cvt_f32_f16_e32 v148, v118
	v_cvt_f32_f16_sdwa v149, v118 dst_sel:DWORD dst_unused:UNUSED_PAD src0_sel:WORD_1
	v_cvt_f32_f16_e32 v150, v119
	v_cvt_f32_f16_sdwa v151, v119 dst_sel:DWORD dst_unused:UNUSED_PAD src0_sel:WORD_1
	v_pk_add_f32 v[4:5], v[4:5], v[144:145]
	v_pk_add_f32 v[6:7], v[6:7], v[146:147]
	v_pk_add_f32 v[8:9], v[8:9], v[148:149]
	v_pk_add_f32 v[10:11], v[10:11], v[150:151]
	s_waitcnt vmcnt(5)
	v_cvt_f32_f16_e32 v144, v120
	v_cvt_f32_f16_sdwa v145, v120 dst_sel:DWORD dst_unused:UNUSED_PAD src0_sel:WORD_1
	v_cvt_f32_f16_e32 v146, v121
	v_cvt_f32_f16_sdwa v147, v121 dst_sel:DWORD dst_unused:UNUSED_PAD src0_sel:WORD_1
	v_cvt_f32_f16_e32 v148, v122
	v_cvt_f32_f16_sdwa v149, v122 dst_sel:DWORD dst_unused:UNUSED_PAD src0_sel:WORD_1
	v_cvt_f32_f16_e32 v150, v123
	v_cvt_f32_f16_sdwa v151, v123 dst_sel:DWORD dst_unused:UNUSED_PAD src0_sel:WORD_1
	v_pk_add_f32 v[4:5], v[4:5], v[144:145]
	v_pk_add_f32 v[6:7], v[6:7], v[146:147]
	v_pk_add_f32 v[8:9], v[8:9], v[148:149]
	v_pk_add_f32 v[10:11], v[10:11], v[150:151]
	s_waitcnt vmcnt(4)
	v_cvt_f32_f16_e32 v144, v124
	v_cvt_f32_f16_sdwa v145, v124 dst_sel:DWORD dst_unused:UNUSED_PAD src0_sel:WORD_1
	v_cvt_f32_f16_e32 v146, v125
	v_cvt_f32_f16_sdwa v147, v125 dst_sel:DWORD dst_unused:UNUSED_PAD src0_sel:WORD_1
	v_cvt_f32_f16_e32 v148, v126
	v_cvt_f32_f16_sdwa v149, v126 dst_sel:DWORD dst_unused:UNUSED_PAD src0_sel:WORD_1
	v_cvt_f32_f16_e32 v150, v127
	v_cvt_f32_f16_sdwa v151, v127 dst_sel:DWORD dst_unused:UNUSED_PAD src0_sel:WORD_1
	v_pk_add_f32 v[4:5], v[4:5], v[144:145]
	v_pk_add_f32 v[6:7], v[6:7], v[146:147]
	v_pk_add_f32 v[8:9], v[8:9], v[148:149]
	v_pk_add_f32 v[10:11], v[10:11], v[150:151]
	s_waitcnt vmcnt(3)
	v_cvt_f32_f16_e32 v144, v128
	v_cvt_f32_f16_sdwa v145, v128 dst_sel:DWORD dst_unused:UNUSED_PAD src0_sel:WORD_1
	v_cvt_f32_f16_e32 v146, v129
	v_cvt_f32_f16_sdwa v147, v129 dst_sel:DWORD dst_unused:UNUSED_PAD src0_sel:WORD_1
	v_cvt_f32_f16_e32 v148, v130
	v_cvt_f32_f16_sdwa v149, v130 dst_sel:DWORD dst_unused:UNUSED_PAD src0_sel:WORD_1
	v_cvt_f32_f16_e32 v150, v131
	v_cvt_f32_f16_sdwa v151, v131 dst_sel:DWORD dst_unused:UNUSED_PAD src0_sel:WORD_1
	v_pk_add_f32 v[4:5], v[4:5], v[144:145]
	v_pk_add_f32 v[6:7], v[6:7], v[146:147]
	v_pk_add_f32 v[8:9], v[8:9], v[148:149]
	v_pk_add_f32 v[10:11], v[10:11], v[150:151]
	s_waitcnt vmcnt(2)
	v_cvt_f32_f16_e32 v144, v132
	v_cvt_f32_f16_sdwa v145, v132 dst_sel:DWORD dst_unused:UNUSED_PAD src0_sel:WORD_1
	v_cvt_f32_f16_e32 v146, v133
	v_cvt_f32_f16_sdwa v147, v133 dst_sel:DWORD dst_unused:UNUSED_PAD src0_sel:WORD_1
	v_cvt_f32_f16_e32 v148, v134
	v_cvt_f32_f16_sdwa v149, v134 dst_sel:DWORD dst_unused:UNUSED_PAD src0_sel:WORD_1
	v_cvt_f32_f16_e32 v150, v135
	v_cvt_f32_f16_sdwa v151, v135 dst_sel:DWORD dst_unused:UNUSED_PAD src0_sel:WORD_1
	v_pk_add_f32 v[4:5], v[4:5], v[144:145]
	v_pk_add_f32 v[6:7], v[6:7], v[146:147]
	v_pk_add_f32 v[8:9], v[8:9], v[148:149]
	v_pk_add_f32 v[10:11], v[10:11], v[150:151]
	s_waitcnt vmcnt(1)
	v_cvt_f32_f16_e32 v144, v136
	v_cvt_f32_f16_sdwa v145, v136 dst_sel:DWORD dst_unused:UNUSED_PAD src0_sel:WORD_1
	v_cvt_f32_f16_e32 v146, v137
	v_cvt_f32_f16_sdwa v147, v137 dst_sel:DWORD dst_unused:UNUSED_PAD src0_sel:WORD_1
	v_cvt_f32_f16_e32 v148, v138
	v_cvt_f32_f16_sdwa v149, v138 dst_sel:DWORD dst_unused:UNUSED_PAD src0_sel:WORD_1
	v_cvt_f32_f16_e32 v150, v139
	v_cvt_f32_f16_sdwa v151, v139 dst_sel:DWORD dst_unused:UNUSED_PAD src0_sel:WORD_1
	v_pk_add_f32 v[4:5], v[4:5], v[144:145]
	v_pk_add_f32 v[6:7], v[6:7], v[146:147]
	v_pk_add_f32 v[8:9], v[8:9], v[148:149]
	v_pk_add_f32 v[10:11], v[10:11], v[150:151]
	s_waitcnt vmcnt(0)
	v_cvt_f32_f16_e32 v144, v140
	v_cvt_f32_f16_sdwa v145, v140 dst_sel:DWORD dst_unused:UNUSED_PAD src0_sel:WORD_1
	v_cvt_f32_f16_e32 v146, v141
	v_cvt_f32_f16_sdwa v147, v141 dst_sel:DWORD dst_unused:UNUSED_PAD src0_sel:WORD_1
	v_cvt_f32_f16_e32 v148, v142
	v_cvt_f32_f16_sdwa v149, v142 dst_sel:DWORD dst_unused:UNUSED_PAD src0_sel:WORD_1
	v_cvt_f32_f16_e32 v150, v143
	v_cvt_f32_f16_sdwa v151, v143 dst_sel:DWORD dst_unused:UNUSED_PAD src0_sel:WORD_1
	v_pk_add_f32 v[4:5], v[4:5], v[144:145]
	v_pk_add_f32 v[6:7], v[6:7], v[146:147]
	v_pk_add_f32 v[8:9], v[8:9], v[148:149]
	v_pk_add_f32 v[10:11], v[10:11], v[150:151]
	v_and_b32_e32 v12, 3, v2
	v_bfe_u32 v13, v2, 2, 6
	v_lshrrev_b32_e32 v14, 8, v2
	v_lshlrev_b32_e32 v14, 5, v14
	v_lshl_add_u32 v14, v12, 3, v14
	v_lshlrev_b32_e32 v14, 8, v14
	v_lshl_add_u32 v14, v13, 2, v14
	v_mul_f32_e32 v152, 0x3b800000, v4
	v_mul_f32_e32 v153, 0x3b800000, v5
	v_mul_f32_e32 v154, 0x3b800000, v6
	v_mul_f32_e32 v155, 0x3b800000, v7
	v_mul_f32_e32 v156, 0x3b800000, v8
	v_mul_f32_e32 v157, 0x3b800000, v9
	v_mul_f32_e32 v158, 0x3b800000, v10
	v_mul_f32_e32 v159, 0x3b800000, v11
	global_store_dword v14, v152, s[6:7]
	global_store_dword v14, v153, s[6:7] offset:256
	global_store_dword v14, v154, s[6:7] offset:512
	global_store_dword v14, v155, s[6:7] offset:768
	global_store_dword v14, v156, s[6:7] offset:1024
	global_store_dword v14, v157, s[6:7] offset:1280
	global_store_dword v14, v158, s[6:7] offset:1536
	global_store_dword v14, v159, s[6:7] offset:1792
.Lk3_exit:
	s_endpgm
	.section	.rodata,"a",@progbits
	.p2align	6, 0x0
	.amdhsa_kernel _Z13reduce_kernelPKDF16_Pf
		.amdhsa_group_segment_fixed_size 0
		.amdhsa_private_segment_fixed_size 0
		.amdhsa_kernarg_size 16
		.amdhsa_user_sgpr_count 2
		.amdhsa_user_sgpr_dispatch_ptr 0
		.amdhsa_user_sgpr_queue_ptr 0
		.amdhsa_user_sgpr_kernarg_segment_ptr 1
		.amdhsa_user_sgpr_dispatch_id 0
		.amdhsa_user_sgpr_kernarg_preload_length 0
		.amdhsa_user_sgpr_kernarg_preload_offset 0
		.amdhsa_user_sgpr_private_segment_size 0
		.amdhsa_uses_dynamic_stack 0
		.amdhsa_enable_private_segment 0
		.amdhsa_system_sgpr_workgroup_id_x 1
		.amdhsa_system_sgpr_workgroup_id_y 0
		.amdhsa_system_sgpr_workgroup_id_z 0
		.amdhsa_system_sgpr_workgroup_info 0
		.amdhsa_system_vgpr_workitem_id 0
		.amdhsa_next_free_vgpr 160
		.amdhsa_next_free_sgpr 19
		.amdhsa_accum_offset 160
		.amdhsa_reserve_vcc 1
		.amdhsa_float_round_mode_32 0
		.amdhsa_float_round_mode_16_64 0
		.amdhsa_float_denorm_mode_32 3
		.amdhsa_float_denorm_mode_16_64 3
		.amdhsa_dx10_clamp 1
		.amdhsa_ieee_mode 1
		.amdhsa_fp16_overflow 0
		.amdhsa_tg_split 0
		.amdhsa_exception_fp_ieee_invalid_op 0
		.amdhsa_exception_fp_denorm_src 0
		.amdhsa_exception_fp_ieee_div_zero 0
		.amdhsa_exception_fp_ieee_overflow 0
		.amdhsa_exception_fp_ieee_underflow 0
		.amdhsa_exception_fp_ieee_inexact 0
		.amdhsa_exception_int_div_zero 0
	.end_amdhsa_kernel

amdhsa.kernels:
  - .agpr_count:     0
    .args:
      - .actual_access:  read_only
        .address_space:  global
        .offset:         0
        .size:           8
        .value_kind:     global_buffer
      - .actual_access:  read_only
        .address_space:  global
        .offset:         8
        .size:           8
        .value_kind:     global_buffer
      - .actual_access:  write_only
        .address_space:  global
        .offset:         16
        .size:           8
        .value_kind:     global_buffer
      - .actual_access:  read_only
        .address_space:  global
        .offset:         24
        .size:           8
        .value_kind:     global_buffer
      - .actual_access:  write_only
        .address_space:  global
        .offset:         32
        .size:           8
        .value_kind:     global_buffer
    .group_segment_fixed_size: 43008
    .kernarg_segment_align: 8
    .kernarg_segment_size: 40
    .language:       OpenCL C
    .language_version:
      - 2
      - 0
    .max_flat_workgroup_size: 256
    .name:           _Z15sim_prep_kernelPKfS0_PDF16_S0_S1_
    .private_segment_fixed_size: 0
    .sgpr_count:     43
    .sgpr_spill_count: 0
    .symbol:         _Z15sim_prep_kernelPKfS0_PDF16_S0_S1_.kd
    .uniform_work_group_size: 1
    .uses_dynamic_stack: false
    .vgpr_count:     124
    .vgpr_spill_count: 0
    .wavefront_size: 64
  - .agpr_count:     0
    .args:
      - .address_space:  global
        .offset:         0
        .size:           8
        .value_kind:     global_buffer
      - .address_space:  global
        .offset:         8
        .size:           8
        .value_kind:     global_buffer
      - .actual_access:  write_only
        .address_space:  global
        .offset:         16
        .size:           8
        .value_kind:     global_buffer
    .group_segment_fixed_size: 114688
    .kernarg_segment_align: 8
    .kernarg_segment_size: 24
    .language:       OpenCL C
    .language_version:
      - 2
      - 0
    .max_flat_workgroup_size: 512
    .name:           _Z9feat_gemmPKDF16_S0_PDF16_
    .private_segment_fixed_size: 0
    .sgpr_count:     53
    .sgpr_spill_count: 0
    .symbol:         _Z9feat_gemmPKDF16_S0_PDF16_.kd
    .uniform_work_group_size: 1
    .uses_dynamic_stack: false
    .vgpr_count:     192
    .vgpr_spill_count: 0
    .wavefront_size: 64
  - .agpr_count:     0
    .args:
      - .actual_access:  read_only
        .address_space:  global
        .offset:         0
        .size:           8
        .value_kind:     global_buffer
      - .actual_access:  write_only
        .address_space:  global
        .offset:         8
        .size:           8
        .value_kind:     global_buffer
    .group_segment_fixed_size: 0
    .kernarg_segment_align: 8
    .kernarg_segment_size: 16
    .language:       OpenCL C
    .language_version:
      - 2
      - 0
    .max_flat_workgroup_size: 256
    .name:           _Z13reduce_kernelPKDF16_Pf
    .private_segment_fixed_size: 0
    .sgpr_count:     25
    .sgpr_spill_count: 0
    .symbol:         _Z13reduce_kernelPKDF16_Pf.kd
    .uniform_work_group_size: 1
    .uses_dynamic_stack: false
    .vgpr_count:     160
    .vgpr_spill_count: 0
    .wavefront_size: 64
